# P1 silu epilogue rewritten: independent packed ops instead of a serial per-element exp/rcp chain
# speedup vs baseline: 1.0058x; 1.0058x over previous
; __device__ __forceinline__ float sigmoid_f(float x) { return __builtin_amdgcn_rcpf(1.0f + __builtin_amdgcn_exp2f(-1.4426950408889634f * x)); }
; template <int ACT> __device__ __forceinline__ float act_f(float v) {
;     template <int ACT, int AUX> __device__ __forceinline__ void run(const f32x4 (&acc)[2][2][4][2], const Unit& uu, int wr, int wc, int fr, int fq) const {
;     ...
;         float rsv[8];
; #pragma unroll
;         for (int i = 0; i < 8; ++i) rsv[i] = ss[row0 + (i >> 2) * HALF + (i & 3) * 16];
;         asm volatile("" ::: "memory");
; #pragma unroll
;         for (int i = 0; i < 8; ++i) rsv[i] = __builtin_amdgcn_rsqf(rsv[i] * (1.0f / cfg::DM) + cfg::RMS_EPS);
;         float cs[2][8]; float mx[2][2];
;         if (AUX == 1) {
; #pragma unroll
;             for (int i = 0; i < 16; ++i) cs[i >> 3][i & 7] = 0.f; }
;         if (AUX == 2) { mx[0][0] = mx[0][1] = mx[1][0] = mx[1][1] = 0.f; }
; #pragma unroll
;         for (int ai = 0; ai < 2; ++ai)
; #pragma unroll
;             for (int m = 0; m < 4; ++m) { const int r = row0 + ai * HALF + m * 16; const float rs = rsv[ai * 4 + m];
;                 bf16_t* rowp = O + (size_t)r * cfg::NC + col0; float s1 = 0.f, s2 = 0.f;
; #pragma unroll
;                 for (int bj = 0; bj < 2; ++bj) { f32x4 v0 = acc[ai][bj][m][0] * rs, v1 = acc[ai][bj][m][1] * rs;
; #pragma unroll
;                     for (int j = 0; j < 4; ++j) { v0[j] = act_f<ACT>(v0[j]); v1[j] = act_f<ACT>(v1[j]); }
;                     if (AUX == 4) {
;                         unsigned q[8];
; #pragma unroll
;                         for (int j = 0; j < 4; ++j) { q[j] = (unsigned)fminf(fmaxf(fmaf(v0[j], 255.0f, 0.5f), 1.0f), 255.0f); q[4 + j] = (unsigned)fminf(fmaxf(fmaf(v1[j], 255.0f, 0.5f), 1.0f), 255.0f); }
;                         u32x2 w8; w8.x = q[0] | (q[1] << 8) | (q[2] << 16) | (q[3] << 24); w8.y = q[4] | (q[5] << 8) | (q[6] << 16) | (q[7] << 24);
;                         __builtin_nontemporal_store(w8, (u32x2*)(g8 + ((size_t)((u.pn - 52) >> 4) * cfg::MT + r) * cfg::DM + ((u.pn - 52) & 15) * BM + wc * 32 + 8 * fq + bj * HALF));
;                     } else {
;                     u32x4 w; w.x = cvt_pk_bf16(v0[0], v0[1]); w.y = cvt_pk_bf16(v0[2], v0[3]); w.z = cvt_pk_bf16(v1[0], v1[1]); w.w = cvt_pk_bf16(v1[2], v1[3]);
;                     __builtin_nontemporal_store(w, (u32x4*)(rowp + bj * HALF)); }
.LBB0_213:
	s_and_b64 vcc, exec, s[46:47]
	s_cbranch_vccz .LBB0_215
	s_waitcnt lgkmcnt(0)
	v_lshl_add_u32 v148, s2, 8, v1
	v_ashrrev_i32_e32 v149, 31, v148
	v_lshl_add_u64 v[150:151], v[148:149], 2, s[22:23]
	global_load_dword v152, v[150:151], off
	global_load_dword v154, v[150:151], off offset:64
	global_load_dword v156, v[150:151], off offset:128
	global_load_dword v158, v[150:151], off offset:192
	global_load_dword v160, v[150:151], off offset:512
	global_load_dword v162, v[150:151], off offset:576
	global_load_dword v164, v[150:151], off offset:640
	global_load_dword v166, v[150:151], off offset:704
	v_lshl_or_b32 v174, s1, 8, v191
	v_lshlrev_b32_e32 v174, 1, v174
	v_mov_b32_e32 v175, 0
	s_mov_b32 s39, 0xe800
	v_mov_b64_e32 v[172:173], s[20:21]
	v_mad_i64_i32 v[172:173], s[12:13], v148, s39, v[172:173]
	v_lshl_add_u64 v[172:173], v[172:173], 0, v[174:175]
	s_mov_b32 s100, 0xe8000
	s_mov_b32 s101, 0
	v_mov_b32_e32 v168, 1.0
	v_mov_b32_e32 v170, 0xbfb8aa3b
	s_waitcnt vmcnt(0)
	v_fmamk_f32 v152, v152, 0x39800000, v221
	v_fmamk_f32 v154, v154, 0x39800000, v221
	v_fmamk_f32 v156, v156, 0x39800000, v221
	v_fmamk_f32 v158, v158, 0x39800000, v221
	v_fmamk_f32 v160, v160, 0x39800000, v221
	v_fmamk_f32 v162, v162, 0x39800000, v221
	v_fmamk_f32 v164, v164, 0x39800000, v221
	v_fmamk_f32 v166, v166, 0x39800000, v221
	v_rsq_f32_e32 v152, v152
	v_rsq_f32_e32 v154, v154
	v_rsq_f32_e32 v156, v156
	v_rsq_f32_e32 v158, v158
	v_rsq_f32_e32 v160, v160
	v_rsq_f32_e32 v162, v162
	v_rsq_f32_e32 v164, v164
	v_rsq_f32_e32 v166, v166
	v_pk_mul_f32 v[128:129], v[128:129], v[152:153] op_sel_hi:[1,0]
	v_pk_mul_f32 v[130:131], v[130:131], v[152:153] op_sel_hi:[1,0]
	v_pk_mul_f32 v[124:125], v[124:125], v[152:153] op_sel_hi:[1,0]
	v_pk_mul_f32 v[126:127], v[126:127], v[152:153] op_sel_hi:[1,0]
	v_pk_mul_f32 v[146:147], v[128:129], v[170:171] op_sel_hi:[1,0]
	v_pk_mul_f32 v[176:177], v[130:131], v[170:171] op_sel_hi:[1,0]
	v_pk_mul_f32 v[178:179], v[124:125], v[170:171] op_sel_hi:[1,0]
	v_pk_mul_f32 v[180:181], v[126:127], v[170:171] op_sel_hi:[1,0]
	v_exp_f32_e32 v146, v146
	v_exp_f32_e32 v147, v147
	v_exp_f32_e32 v176, v176
	v_exp_f32_e32 v177, v177
	v_exp_f32_e32 v178, v178
	v_exp_f32_e32 v179, v179
	v_exp_f32_e32 v180, v180
	v_exp_f32_e32 v181, v181
	v_pk_add_f32 v[146:147], v[146:147], v[168:169] op_sel_hi:[1,0]
	v_pk_add_f32 v[176:177], v[176:177], v[168:169] op_sel_hi:[1,0]
	v_pk_add_f32 v[178:179], v[178:179], v[168:169] op_sel_hi:[1,0]
	v_pk_add_f32 v[180:181], v[180:181], v[168:169] op_sel_hi:[1,0]
	v_rcp_f32_e32 v146, v146
	v_rcp_f32_e32 v147, v147
	v_rcp_f32_e32 v176, v176
	v_rcp_f32_e32 v177, v177
	v_rcp_f32_e32 v178, v178
	v_rcp_f32_e32 v179, v179
	v_rcp_f32_e32 v180, v180
	v_rcp_f32_e32 v181, v181
	v_pk_mul_f32 v[128:129], v[128:129], v[146:147]
	v_pk_mul_f32 v[130:131], v[130:131], v[176:177]
	v_pk_mul_f32 v[124:125], v[124:125], v[178:179]
	v_pk_mul_f32 v[126:127], v[126:127], v[180:181]
	v_cvt_pk_bf16_f32 v128, v128, v129
	v_cvt_pk_bf16_f32 v129, v130, v131
	v_cvt_pk_bf16_f32 v130, v124, v125
	v_cvt_pk_bf16_f32 v131, v126, v127
	global_store_dwordx4 v[172:173], v[128:131], off nt
	v_pk_mul_f32 v[120:121], v[120:121], v[152:153] op_sel_hi:[1,0]
	v_pk_mul_f32 v[122:123], v[122:123], v[152:153] op_sel_hi:[1,0]
	v_pk_mul_f32 v[116:117], v[116:117], v[152:153] op_sel_hi:[1,0]
	v_pk_mul_f32 v[118:119], v[118:119], v[152:153] op_sel_hi:[1,0]
	v_pk_mul_f32 v[146:147], v[120:121], v[170:171] op_sel_hi:[1,0]
	v_pk_mul_f32 v[176:177], v[122:123], v[170:171] op_sel_hi:[1,0]
	v_pk_mul_f32 v[178:179], v[116:117], v[170:171] op_sel_hi:[1,0]
	v_pk_mul_f32 v[180:181], v[118:119], v[170:171] op_sel_hi:[1,0]
	v_exp_f32_e32 v146, v146
	v_exp_f32_e32 v147, v147
	v_exp_f32_e32 v176, v176
	v_exp_f32_e32 v177, v177
	v_exp_f32_e32 v178, v178
	v_exp_f32_e32 v179, v179
	v_exp_f32_e32 v180, v180
	v_exp_f32_e32 v181, v181
	v_pk_add_f32 v[146:147], v[146:147], v[168:169] op_sel_hi:[1,0]
	v_pk_add_f32 v[176:177], v[176:177], v[168:169] op_sel_hi:[1,0]
	v_pk_add_f32 v[178:179], v[178:179], v[168:169] op_sel_hi:[1,0]
	v_pk_add_f32 v[180:181], v[180:181], v[168:169] op_sel_hi:[1,0]
	v_rcp_f32_e32 v146, v146
	v_rcp_f32_e32 v147, v147
	v_rcp_f32_e32 v176, v176
	v_rcp_f32_e32 v177, v177
	v_rcp_f32_e32 v178, v178
	v_rcp_f32_e32 v179, v179
	v_rcp_f32_e32 v180, v180
	v_rcp_f32_e32 v181, v181
	v_pk_mul_f32 v[120:121], v[120:121], v[146:147]
	v_pk_mul_f32 v[122:123], v[122:123], v[176:177]
	v_pk_mul_f32 v[116:117], v[116:117], v[178:179]
	v_pk_mul_f32 v[118:119], v[118:119], v[180:181]
	v_cvt_pk_bf16_f32 v120, v120, v121
	v_cvt_pk_bf16_f32 v121, v122, v123
	v_cvt_pk_bf16_f32 v122, v116, v117
	v_cvt_pk_bf16_f32 v123, v118, v119
	global_store_dwordx4 v[172:173], v[120:123], off offset:256 nt
	v_lshl_add_u64 v[174:175], v[172:173], 0, s[100:101]
	v_pk_mul_f32 v[112:113], v[112:113], v[154:155] op_sel_hi:[1,0]
	v_pk_mul_f32 v[114:115], v[114:115], v[154:155] op_sel_hi:[1,0]
	v_pk_mul_f32 v[108:109], v[108:109], v[154:155] op_sel_hi:[1,0]
	v_pk_mul_f32 v[110:111], v[110:111], v[154:155] op_sel_hi:[1,0]
	v_pk_mul_f32 v[146:147], v[112:113], v[170:171] op_sel_hi:[1,0]
	v_pk_mul_f32 v[176:177], v[114:115], v[170:171] op_sel_hi:[1,0]
	v_pk_mul_f32 v[178:179], v[108:109], v[170:171] op_sel_hi:[1,0]
	v_pk_mul_f32 v[180:181], v[110:111], v[170:171] op_sel_hi:[1,0]
	v_exp_f32_e32 v146, v146
	v_exp_f32_e32 v147, v147
	v_exp_f32_e32 v176, v176
	v_exp_f32_e32 v177, v177
	v_exp_f32_e32 v178, v178
	v_exp_f32_e32 v179, v179
	v_exp_f32_e32 v180, v180
	v_exp_f32_e32 v181, v181
	v_pk_add_f32 v[146:147], v[146:147], v[168:169] op_sel_hi:[1,0]
	v_pk_add_f32 v[176:177], v[176:177], v[168:169] op_sel_hi:[1,0]
; __device__ __forceinline__ unsigned cvt_pk_bf16(float lo, float hi) { f32x2_t v = {lo, hi}; bf16x2_t b = __builtin_convertvector(v, bf16x2_t); return __builtin_bit_cast(unsigned, b); }
; __device__ __forceinline__ float sigmoid_f(float x) { return __builtin_amdgcn_rcpf(1.0f + __builtin_amdgcn_exp2f(-1.4426950408889634f * x)); }
; template <int ACT> __device__ __forceinline__ float act_f(float v) {
;     if (ACT == 1) return v * sigmoid_f(v);
;     template <int ACT, int AUX> __device__ __forceinline__ void run(const f32x4 (&acc)[2][2][4][2], const Unit& uu, int wr, int wc, int fr, int fq) const {
;     ...
;             for (int m = 0; m < 4; ++m) { const int r = row0 + ai * HALF + m * 16; const float rs = rsv[ai * 4 + m];
;                 bf16_t* rowp = O + (size_t)r * cfg::NC + col0; float s1 = 0.f, s2 = 0.f;
; #pragma unroll
;                 for (int bj = 0; bj < 2; ++bj) { f32x4 v0 = acc[ai][bj][m][0] * rs, v1 = acc[ai][bj][m][1] * rs;
; #pragma unroll
;                     for (int j = 0; j < 4; ++j) { v0[j] = act_f<ACT>(v0[j]); v1[j] = act_f<ACT>(v1[j]); }
;                     if (AUX == 4) {
;                         unsigned q[8];
; #pragma unroll
;                         for (int j = 0; j < 4; ++j) { q[j] = (unsigned)fminf(fmaxf(fmaf(v0[j], 255.0f, 0.5f), 1.0f), 255.0f); q[4 + j] = (unsigned)fminf(fmaxf(fmaf(v1[j], 255.0f, 0.5f), 1.0f), 255.0f); }
;                         u32x2 w8; w8.x = q[0] | (q[1] << 8) | (q[2] << 16) | (q[3] << 24); w8.y = q[4] | (q[5] << 8) | (q[6] << 16) | (q[7] << 24);
;                         __builtin_nontemporal_store(w8, (u32x2*)(g8 + ((size_t)((u.pn - 52) >> 4) * cfg::MT + r) * cfg::DM + ((u.pn - 52) & 15) * BM + wc * 32 + 8 * fq + bj * HALF));
;                     } else {
;                     u32x4 w; w.x = cvt_pk_bf16(v0[0], v0[1]); w.y = cvt_pk_bf16(v0[2], v0[3]); w.z = cvt_pk_bf16(v1[0], v1[1]); w.w = cvt_pk_bf16(v1[2], v1[3]);
;                     __builtin_nontemporal_store(w, (u32x4*)(rowp + bj * HALF)); }
	v_pk_add_f32 v[178:179], v[178:179], v[168:169] op_sel_hi:[1,0]
	v_pk_add_f32 v[180:181], v[180:181], v[168:169] op_sel_hi:[1,0]
	v_rcp_f32_e32 v146, v146
	v_rcp_f32_e32 v147, v147
	v_rcp_f32_e32 v176, v176
	v_rcp_f32_e32 v177, v177
	v_rcp_f32_e32 v178, v178
	v_rcp_f32_e32 v179, v179
	v_rcp_f32_e32 v180, v180
	v_rcp_f32_e32 v181, v181
	v_pk_mul_f32 v[112:113], v[112:113], v[146:147]
	v_pk_mul_f32 v[114:115], v[114:115], v[176:177]
	v_pk_mul_f32 v[108:109], v[108:109], v[178:179]
	v_pk_mul_f32 v[110:111], v[110:111], v[180:181]
	v_cvt_pk_bf16_f32 v112, v112, v113
	v_cvt_pk_bf16_f32 v113, v114, v115
	v_cvt_pk_bf16_f32 v114, v108, v109
	v_cvt_pk_bf16_f32 v115, v110, v111
	global_store_dwordx4 v[174:175], v[112:115], off nt
	v_pk_mul_f32 v[104:105], v[104:105], v[154:155] op_sel_hi:[1,0]
	v_pk_mul_f32 v[106:107], v[106:107], v[154:155] op_sel_hi:[1,0]
	v_pk_mul_f32 v[100:101], v[100:101], v[154:155] op_sel_hi:[1,0]
	v_pk_mul_f32 v[102:103], v[102:103], v[154:155] op_sel_hi:[1,0]
	v_pk_mul_f32 v[146:147], v[104:105], v[170:171] op_sel_hi:[1,0]
	v_pk_mul_f32 v[176:177], v[106:107], v[170:171] op_sel_hi:[1,0]
	v_pk_mul_f32 v[178:179], v[100:101], v[170:171] op_sel_hi:[1,0]
	v_pk_mul_f32 v[180:181], v[102:103], v[170:171] op_sel_hi:[1,0]
	v_exp_f32_e32 v146, v146
	v_exp_f32_e32 v147, v147
	v_exp_f32_e32 v176, v176
	v_exp_f32_e32 v177, v177
	v_exp_f32_e32 v178, v178
	v_exp_f32_e32 v179, v179
	v_exp_f32_e32 v180, v180
	v_exp_f32_e32 v181, v181
	v_pk_add_f32 v[146:147], v[146:147], v[168:169] op_sel_hi:[1,0]
	v_pk_add_f32 v[176:177], v[176:177], v[168:169] op_sel_hi:[1,0]
	v_pk_add_f32 v[178:179], v[178:179], v[168:169] op_sel_hi:[1,0]
	v_pk_add_f32 v[180:181], v[180:181], v[168:169] op_sel_hi:[1,0]
	v_rcp_f32_e32 v146, v146
	v_rcp_f32_e32 v147, v147
	v_rcp_f32_e32 v176, v176
	v_rcp_f32_e32 v177, v177
	v_rcp_f32_e32 v178, v178
	v_rcp_f32_e32 v179, v179
	v_rcp_f32_e32 v180, v180
	v_rcp_f32_e32 v181, v181
	v_pk_mul_f32 v[104:105], v[104:105], v[146:147]
	v_pk_mul_f32 v[106:107], v[106:107], v[176:177]
	v_pk_mul_f32 v[100:101], v[100:101], v[178:179]
	v_pk_mul_f32 v[102:103], v[102:103], v[180:181]
	v_cvt_pk_bf16_f32 v104, v104, v105
	v_cvt_pk_bf16_f32 v105, v106, v107
	v_cvt_pk_bf16_f32 v106, v100, v101
	v_cvt_pk_bf16_f32 v107, v102, v103
	global_store_dwordx4 v[174:175], v[104:107], off offset:256 nt
	v_lshl_add_u64 v[172:173], v[174:175], 0, s[100:101]
	v_pk_mul_f32 v[96:97], v[96:97], v[156:157] op_sel_hi:[1,0]
	v_pk_mul_f32 v[98:99], v[98:99], v[156:157] op_sel_hi:[1,0]
	v_pk_mul_f32 v[92:93], v[92:93], v[156:157] op_sel_hi:[1,0]
	v_pk_mul_f32 v[94:95], v[94:95], v[156:157] op_sel_hi:[1,0]
	v_pk_mul_f32 v[146:147], v[96:97], v[170:171] op_sel_hi:[1,0]
	v_pk_mul_f32 v[176:177], v[98:99], v[170:171] op_sel_hi:[1,0]
	v_pk_mul_f32 v[178:179], v[92:93], v[170:171] op_sel_hi:[1,0]
	v_pk_mul_f32 v[180:181], v[94:95], v[170:171] op_sel_hi:[1,0]
	v_exp_f32_e32 v146, v146
	v_exp_f32_e32 v147, v147
	v_exp_f32_e32 v176, v176
	v_exp_f32_e32 v177, v177
	v_exp_f32_e32 v178, v178
	v_exp_f32_e32 v179, v179
	v_exp_f32_e32 v180, v180
	v_exp_f32_e32 v181, v181
	v_pk_add_f32 v[146:147], v[146:147], v[168:169] op_sel_hi:[1,0]
	v_pk_add_f32 v[176:177], v[176:177], v[168:169] op_sel_hi:[1,0]
	v_pk_add_f32 v[178:179], v[178:179], v[168:169] op_sel_hi:[1,0]
	v_pk_add_f32 v[180:181], v[180:181], v[168:169] op_sel_hi:[1,0]
	v_rcp_f32_e32 v146, v146
	v_rcp_f32_e32 v147, v147
	v_rcp_f32_e32 v176, v176
	v_rcp_f32_e32 v177, v177
	v_rcp_f32_e32 v178, v178
	v_rcp_f32_e32 v179, v179
	v_rcp_f32_e32 v180, v180
	v_rcp_f32_e32 v181, v181
	v_pk_mul_f32 v[96:97], v[96:97], v[146:147]
	v_pk_mul_f32 v[98:99], v[98:99], v[176:177]
	v_pk_mul_f32 v[92:93], v[92:93], v[178:179]
	v_pk_mul_f32 v[94:95], v[94:95], v[180:181]
	v_cvt_pk_bf16_f32 v96, v96, v97
	v_cvt_pk_bf16_f32 v97, v98, v99
	v_cvt_pk_bf16_f32 v98, v92, v93
	v_cvt_pk_bf16_f32 v99, v94, v95
	global_store_dwordx4 v[172:173], v[96:99], off nt
	v_pk_mul_f32 v[88:89], v[88:89], v[156:157] op_sel_hi:[1,0]
	v_pk_mul_f32 v[90:91], v[90:91], v[156:157] op_sel_hi:[1,0]
	v_pk_mul_f32 v[84:85], v[84:85], v[156:157] op_sel_hi:[1,0]
	v_pk_mul_f32 v[86:87], v[86:87], v[156:157] op_sel_hi:[1,0]
	v_pk_mul_f32 v[146:147], v[88:89], v[170:171] op_sel_hi:[1,0]
	v_pk_mul_f32 v[176:177], v[90:91], v[170:171] op_sel_hi:[1,0]
	v_pk_mul_f32 v[178:179], v[84:85], v[170:171] op_sel_hi:[1,0]
	v_pk_mul_f32 v[180:181], v[86:87], v[170:171] op_sel_hi:[1,0]
	v_exp_f32_e32 v146, v146
	v_exp_f32_e32 v147, v147
	v_exp_f32_e32 v176, v176
	v_exp_f32_e32 v177, v177
	v_exp_f32_e32 v178, v178
	v_exp_f32_e32 v179, v179
	v_exp_f32_e32 v180, v180
	v_exp_f32_e32 v181, v181
	v_pk_add_f32 v[146:147], v[146:147], v[168:169] op_sel_hi:[1,0]
	v_pk_add_f32 v[176:177], v[176:177], v[168:169] op_sel_hi:[1,0]
	v_pk_add_f32 v[178:179], v[178:179], v[168:169] op_sel_hi:[1,0]
	v_pk_add_f32 v[180:181], v[180:181], v[168:169] op_sel_hi:[1,0]
	v_rcp_f32_e32 v146, v146
	v_rcp_f32_e32 v147, v147
	v_rcp_f32_e32 v176, v176
	v_rcp_f32_e32 v177, v177
	v_rcp_f32_e32 v178, v178
	v_rcp_f32_e32 v179, v179
	v_rcp_f32_e32 v180, v180
	v_rcp_f32_e32 v181, v181
	v_pk_mul_f32 v[88:89], v[88:89], v[146:147]
	v_pk_mul_f32 v[90:91], v[90:91], v[176:177]
	v_pk_mul_f32 v[84:85], v[84:85], v[178:179]
	v_pk_mul_f32 v[86:87], v[86:87], v[180:181]
	v_cvt_pk_bf16_f32 v88, v88, v89
	v_cvt_pk_bf16_f32 v89, v90, v91
	v_cvt_pk_bf16_f32 v90, v84, v85
	v_cvt_pk_bf16_f32 v91, v86, v87
	global_store_dwordx4 v[172:173], v[88:91], off offset:256 nt
	v_lshl_add_u64 v[174:175], v[172:173], 0, s[100:101]
	v_pk_mul_f32 v[80:81], v[80:81], v[158:159] op_sel_hi:[1,0]
	v_pk_mul_f32 v[82:83], v[82:83], v[158:159] op_sel_hi:[1,0]
; __device__ __forceinline__ unsigned cvt_pk_bf16(float lo, float hi) { f32x2_t v = {lo, hi}; bf16x2_t b = __builtin_convertvector(v, bf16x2_t); return __builtin_bit_cast(unsigned, b); }
; __device__ __forceinline__ float sigmoid_f(float x) { return __builtin_amdgcn_rcpf(1.0f + __builtin_amdgcn_exp2f(-1.4426950408889634f * x)); }
; template <int ACT> __device__ __forceinline__ float act_f(float v) {
;     if (ACT == 1) return v * sigmoid_f(v);
;     template <int ACT, int AUX> __device__ __forceinline__ void run(const f32x4 (&acc)[2][2][4][2], const Unit& uu, int wr, int wc, int fr, int fq) const {
;     ...
;             for (int m = 0; m < 4; ++m) { const int r = row0 + ai * HALF + m * 16; const float rs = rsv[ai * 4 + m];
;                 bf16_t* rowp = O + (size_t)r * cfg::NC + col0; float s1 = 0.f, s2 = 0.f;
; #pragma unroll
;                 for (int bj = 0; bj < 2; ++bj) { f32x4 v0 = acc[ai][bj][m][0] * rs, v1 = acc[ai][bj][m][1] * rs;
; #pragma unroll
;                     for (int j = 0; j < 4; ++j) { v0[j] = act_f<ACT>(v0[j]); v1[j] = act_f<ACT>(v1[j]); }
;                     if (AUX == 4) {
;                         unsigned q[8];
; #pragma unroll
;                         for (int j = 0; j < 4; ++j) { q[j] = (unsigned)fminf(fmaxf(fmaf(v0[j], 255.0f, 0.5f), 1.0f), 255.0f); q[4 + j] = (unsigned)fminf(fmaxf(fmaf(v1[j], 255.0f, 0.5f), 1.0f), 255.0f); }
;                         u32x2 w8; w8.x = q[0] | (q[1] << 8) | (q[2] << 16) | (q[3] << 24); w8.y = q[4] | (q[5] << 8) | (q[6] << 16) | (q[7] << 24);
;                         __builtin_nontemporal_store(w8, (u32x2*)(g8 + ((size_t)((u.pn - 52) >> 4) * cfg::MT + r) * cfg::DM + ((u.pn - 52) & 15) * BM + wc * 32 + 8 * fq + bj * HALF));
;                     } else {
;                     u32x4 w; w.x = cvt_pk_bf16(v0[0], v0[1]); w.y = cvt_pk_bf16(v0[2], v0[3]); w.z = cvt_pk_bf16(v1[0], v1[1]); w.w = cvt_pk_bf16(v1[2], v1[3]);
;                     __builtin_nontemporal_store(w, (u32x4*)(rowp + bj * HALF)); }
	v_pk_mul_f32 v[76:77], v[76:77], v[158:159] op_sel_hi:[1,0]
	v_pk_mul_f32 v[78:79], v[78:79], v[158:159] op_sel_hi:[1,0]
	v_pk_mul_f32 v[146:147], v[80:81], v[170:171] op_sel_hi:[1,0]
	v_pk_mul_f32 v[176:177], v[82:83], v[170:171] op_sel_hi:[1,0]
	v_pk_mul_f32 v[178:179], v[76:77], v[170:171] op_sel_hi:[1,0]
	v_pk_mul_f32 v[180:181], v[78:79], v[170:171] op_sel_hi:[1,0]
	v_exp_f32_e32 v146, v146
	v_exp_f32_e32 v147, v147
	v_exp_f32_e32 v176, v176
	v_exp_f32_e32 v177, v177
	v_exp_f32_e32 v178, v178
	v_exp_f32_e32 v179, v179
	v_exp_f32_e32 v180, v180
	v_exp_f32_e32 v181, v181
	v_pk_add_f32 v[146:147], v[146:147], v[168:169] op_sel_hi:[1,0]
	v_pk_add_f32 v[176:177], v[176:177], v[168:169] op_sel_hi:[1,0]
	v_pk_add_f32 v[178:179], v[178:179], v[168:169] op_sel_hi:[1,0]
	v_pk_add_f32 v[180:181], v[180:181], v[168:169] op_sel_hi:[1,0]
	v_rcp_f32_e32 v146, v146
	v_rcp_f32_e32 v147, v147
	v_rcp_f32_e32 v176, v176
	v_rcp_f32_e32 v177, v177
	v_rcp_f32_e32 v178, v178
	v_rcp_f32_e32 v179, v179
	v_rcp_f32_e32 v180, v180
	v_rcp_f32_e32 v181, v181
	v_pk_mul_f32 v[80:81], v[80:81], v[146:147]
	v_pk_mul_f32 v[82:83], v[82:83], v[176:177]
	v_pk_mul_f32 v[76:77], v[76:77], v[178:179]
	v_pk_mul_f32 v[78:79], v[78:79], v[180:181]
	v_cvt_pk_bf16_f32 v80, v80, v81
	v_cvt_pk_bf16_f32 v81, v82, v83
	v_cvt_pk_bf16_f32 v82, v76, v77
	v_cvt_pk_bf16_f32 v83, v78, v79
	global_store_dwordx4 v[174:175], v[80:83], off nt
	v_pk_mul_f32 v[72:73], v[72:73], v[158:159] op_sel_hi:[1,0]
	v_pk_mul_f32 v[74:75], v[74:75], v[158:159] op_sel_hi:[1,0]
	v_pk_mul_f32 v[68:69], v[68:69], v[158:159] op_sel_hi:[1,0]
	v_pk_mul_f32 v[70:71], v[70:71], v[158:159] op_sel_hi:[1,0]
	v_pk_mul_f32 v[146:147], v[72:73], v[170:171] op_sel_hi:[1,0]
	v_pk_mul_f32 v[176:177], v[74:75], v[170:171] op_sel_hi:[1,0]
	v_pk_mul_f32 v[178:179], v[68:69], v[170:171] op_sel_hi:[1,0]
	v_pk_mul_f32 v[180:181], v[70:71], v[170:171] op_sel_hi:[1,0]
	v_exp_f32_e32 v146, v146
	v_exp_f32_e32 v147, v147
	v_exp_f32_e32 v176, v176
	v_exp_f32_e32 v177, v177
	v_exp_f32_e32 v178, v178
	v_exp_f32_e32 v179, v179
	v_exp_f32_e32 v180, v180
	v_exp_f32_e32 v181, v181
	v_pk_add_f32 v[146:147], v[146:147], v[168:169] op_sel_hi:[1,0]
	v_pk_add_f32 v[176:177], v[176:177], v[168:169] op_sel_hi:[1,0]
	v_pk_add_f32 v[178:179], v[178:179], v[168:169] op_sel_hi:[1,0]
	v_pk_add_f32 v[180:181], v[180:181], v[168:169] op_sel_hi:[1,0]
	v_rcp_f32_e32 v146, v146
	v_rcp_f32_e32 v147, v147
	v_rcp_f32_e32 v176, v176
	v_rcp_f32_e32 v177, v177
	v_rcp_f32_e32 v178, v178
	v_rcp_f32_e32 v179, v179
	v_rcp_f32_e32 v180, v180
	v_rcp_f32_e32 v181, v181
	v_pk_mul_f32 v[72:73], v[72:73], v[146:147]
	v_pk_mul_f32 v[74:75], v[74:75], v[176:177]
	v_pk_mul_f32 v[68:69], v[68:69], v[178:179]
	v_pk_mul_f32 v[70:71], v[70:71], v[180:181]
	v_cvt_pk_bf16_f32 v72, v72, v73
	v_cvt_pk_bf16_f32 v73, v74, v75
	v_cvt_pk_bf16_f32 v74, v68, v69
	v_cvt_pk_bf16_f32 v75, v70, v71
	global_store_dwordx4 v[174:175], v[72:75], off offset:256 nt
	s_mov_b32 s100, 0x488000
	v_lshl_add_u64 v[172:173], v[174:175], 0, s[100:101]
	s_mov_b32 s100, 0xe8000
	v_pk_mul_f32 v[64:65], v[64:65], v[160:161] op_sel_hi:[1,0]
	v_pk_mul_f32 v[66:67], v[66:67], v[160:161] op_sel_hi:[1,0]
	v_pk_mul_f32 v[60:61], v[60:61], v[160:161] op_sel_hi:[1,0]
	v_pk_mul_f32 v[62:63], v[62:63], v[160:161] op_sel_hi:[1,0]
	v_pk_mul_f32 v[146:147], v[64:65], v[170:171] op_sel_hi:[1,0]
	v_pk_mul_f32 v[176:177], v[66:67], v[170:171] op_sel_hi:[1,0]
	v_pk_mul_f32 v[178:179], v[60:61], v[170:171] op_sel_hi:[1,0]
	v_pk_mul_f32 v[180:181], v[62:63], v[170:171] op_sel_hi:[1,0]
	v_exp_f32_e32 v146, v146
	v_exp_f32_e32 v147, v147
	v_exp_f32_e32 v176, v176
	v_exp_f32_e32 v177, v177
	v_exp_f32_e32 v178, v178
	v_exp_f32_e32 v179, v179
	v_exp_f32_e32 v180, v180
	v_exp_f32_e32 v181, v181
	v_pk_add_f32 v[146:147], v[146:147], v[168:169] op_sel_hi:[1,0]
	v_pk_add_f32 v[176:177], v[176:177], v[168:169] op_sel_hi:[1,0]
	v_pk_add_f32 v[178:179], v[178:179], v[168:169] op_sel_hi:[1,0]
	v_pk_add_f32 v[180:181], v[180:181], v[168:169] op_sel_hi:[1,0]
	v_rcp_f32_e32 v146, v146
	v_rcp_f32_e32 v147, v147
	v_rcp_f32_e32 v176, v176
	v_rcp_f32_e32 v177, v177
	v_rcp_f32_e32 v178, v178
	v_rcp_f32_e32 v179, v179
	v_rcp_f32_e32 v180, v180
	v_rcp_f32_e32 v181, v181
	v_pk_mul_f32 v[64:65], v[64:65], v[146:147]
	v_pk_mul_f32 v[66:67], v[66:67], v[176:177]
	v_pk_mul_f32 v[60:61], v[60:61], v[178:179]
	v_pk_mul_f32 v[62:63], v[62:63], v[180:181]
	v_cvt_pk_bf16_f32 v64, v64, v65
	v_cvt_pk_bf16_f32 v65, v66, v67
	v_cvt_pk_bf16_f32 v66, v60, v61
	v_cvt_pk_bf16_f32 v67, v62, v63
	global_store_dwordx4 v[172:173], v[64:67], off nt
	v_pk_mul_f32 v[56:57], v[56:57], v[160:161] op_sel_hi:[1,0]
	v_pk_mul_f32 v[58:59], v[58:59], v[160:161] op_sel_hi:[1,0]
	v_pk_mul_f32 v[52:53], v[52:53], v[160:161] op_sel_hi:[1,0]
	v_pk_mul_f32 v[54:55], v[54:55], v[160:161] op_sel_hi:[1,0]
	v_pk_mul_f32 v[146:147], v[56:57], v[170:171] op_sel_hi:[1,0]
	v_pk_mul_f32 v[176:177], v[58:59], v[170:171] op_sel_hi:[1,0]
	v_pk_mul_f32 v[178:179], v[52:53], v[170:171] op_sel_hi:[1,0]
	v_pk_mul_f32 v[180:181], v[54:55], v[170:171] op_sel_hi:[1,0]
	v_exp_f32_e32 v146, v146
	v_exp_f32_e32 v147, v147
	v_exp_f32_e32 v176, v176
	v_exp_f32_e32 v177, v177
	v_exp_f32_e32 v178, v178
	v_exp_f32_e32 v179, v179
	v_exp_f32_e32 v180, v180
	v_exp_f32_e32 v181, v181
	v_pk_add_f32 v[146:147], v[146:147], v[168:169] op_sel_hi:[1,0]
	v_pk_add_f32 v[176:177], v[176:177], v[168:169] op_sel_hi:[1,0]
	v_pk_add_f32 v[178:179], v[178:179], v[168:169] op_sel_hi:[1,0]
	v_pk_add_f32 v[180:181], v[180:181], v[168:169] op_sel_hi:[1,0]
	v_rcp_f32_e32 v146, v146
	v_rcp_f32_e32 v147, v147
	v_rcp_f32_e32 v176, v176
; __device__ __forceinline__ unsigned cvt_pk_bf16(float lo, float hi) { f32x2_t v = {lo, hi}; bf16x2_t b = __builtin_convertvector(v, bf16x2_t); return __builtin_bit_cast(unsigned, b); }
; __device__ __forceinline__ float sigmoid_f(float x) { return __builtin_amdgcn_rcpf(1.0f + __builtin_amdgcn_exp2f(-1.4426950408889634f * x)); }
; template <int ACT> __device__ __forceinline__ float act_f(float v) {
;     if (ACT == 1) return v * sigmoid_f(v);
;     template <int ACT, int AUX> __device__ __forceinline__ void run(const f32x4 (&acc)[2][2][4][2], const Unit& uu, int wr, int wc, int fr, int fq) const {
;     ...
;             for (int m = 0; m < 4; ++m) { const int r = row0 + ai * HALF + m * 16; const float rs = rsv[ai * 4 + m];
;                 bf16_t* rowp = O + (size_t)r * cfg::NC + col0; float s1 = 0.f, s2 = 0.f;
; #pragma unroll
;                 for (int bj = 0; bj < 2; ++bj) { f32x4 v0 = acc[ai][bj][m][0] * rs, v1 = acc[ai][bj][m][1] * rs;
; #pragma unroll
;                     for (int j = 0; j < 4; ++j) { v0[j] = act_f<ACT>(v0[j]); v1[j] = act_f<ACT>(v1[j]); }
;                     if (AUX == 4) {
;                         unsigned q[8];
; #pragma unroll
;                         for (int j = 0; j < 4; ++j) { q[j] = (unsigned)fminf(fmaxf(fmaf(v0[j], 255.0f, 0.5f), 1.0f), 255.0f); q[4 + j] = (unsigned)fminf(fmaxf(fmaf(v1[j], 255.0f, 0.5f), 1.0f), 255.0f); }
;                         u32x2 w8; w8.x = q[0] | (q[1] << 8) | (q[2] << 16) | (q[3] << 24); w8.y = q[4] | (q[5] << 8) | (q[6] << 16) | (q[7] << 24);
;                         __builtin_nontemporal_store(w8, (u32x2*)(g8 + ((size_t)((u.pn - 52) >> 4) * cfg::MT + r) * cfg::DM + ((u.pn - 52) & 15) * BM + wc * 32 + 8 * fq + bj * HALF));
;                     } else {
;                     u32x4 w; w.x = cvt_pk_bf16(v0[0], v0[1]); w.y = cvt_pk_bf16(v0[2], v0[3]); w.z = cvt_pk_bf16(v1[0], v1[1]); w.w = cvt_pk_bf16(v1[2], v1[3]);
;                     __builtin_nontemporal_store(w, (u32x4*)(rowp + bj * HALF)); }
	v_rcp_f32_e32 v177, v177
	v_rcp_f32_e32 v178, v178
	v_rcp_f32_e32 v179, v179
	v_rcp_f32_e32 v180, v180
	v_rcp_f32_e32 v181, v181
	v_pk_mul_f32 v[56:57], v[56:57], v[146:147]
	v_pk_mul_f32 v[58:59], v[58:59], v[176:177]
	v_pk_mul_f32 v[52:53], v[52:53], v[178:179]
	v_pk_mul_f32 v[54:55], v[54:55], v[180:181]
	v_cvt_pk_bf16_f32 v56, v56, v57
	v_cvt_pk_bf16_f32 v57, v58, v59
	v_cvt_pk_bf16_f32 v58, v52, v53
	v_cvt_pk_bf16_f32 v59, v54, v55
	global_store_dwordx4 v[172:173], v[56:59], off offset:256 nt
	v_lshl_add_u64 v[174:175], v[172:173], 0, s[100:101]
	v_pk_mul_f32 v[48:49], v[48:49], v[162:163] op_sel_hi:[1,0]
	v_pk_mul_f32 v[50:51], v[50:51], v[162:163] op_sel_hi:[1,0]
	v_pk_mul_f32 v[44:45], v[44:45], v[162:163] op_sel_hi:[1,0]
	v_pk_mul_f32 v[46:47], v[46:47], v[162:163] op_sel_hi:[1,0]
	v_pk_mul_f32 v[146:147], v[48:49], v[170:171] op_sel_hi:[1,0]
	v_pk_mul_f32 v[176:177], v[50:51], v[170:171] op_sel_hi:[1,0]
	v_pk_mul_f32 v[178:179], v[44:45], v[170:171] op_sel_hi:[1,0]
	v_pk_mul_f32 v[180:181], v[46:47], v[170:171] op_sel_hi:[1,0]
	v_exp_f32_e32 v146, v146
	v_exp_f32_e32 v147, v147
	v_exp_f32_e32 v176, v176
	v_exp_f32_e32 v177, v177
	v_exp_f32_e32 v178, v178
	v_exp_f32_e32 v179, v179
	v_exp_f32_e32 v180, v180
	v_exp_f32_e32 v181, v181
	v_pk_add_f32 v[146:147], v[146:147], v[168:169] op_sel_hi:[1,0]
	v_pk_add_f32 v[176:177], v[176:177], v[168:169] op_sel_hi:[1,0]
	v_pk_add_f32 v[178:179], v[178:179], v[168:169] op_sel_hi:[1,0]
	v_pk_add_f32 v[180:181], v[180:181], v[168:169] op_sel_hi:[1,0]
	v_rcp_f32_e32 v146, v146
	v_rcp_f32_e32 v147, v147
	v_rcp_f32_e32 v176, v176
	v_rcp_f32_e32 v177, v177
	v_rcp_f32_e32 v178, v178
	v_rcp_f32_e32 v179, v179
	v_rcp_f32_e32 v180, v180
	v_rcp_f32_e32 v181, v181
	v_pk_mul_f32 v[48:49], v[48:49], v[146:147]
	v_pk_mul_f32 v[50:51], v[50:51], v[176:177]
	v_pk_mul_f32 v[44:45], v[44:45], v[178:179]
	v_pk_mul_f32 v[46:47], v[46:47], v[180:181]
	v_cvt_pk_bf16_f32 v48, v48, v49
	v_cvt_pk_bf16_f32 v49, v50, v51
	v_cvt_pk_bf16_f32 v50, v44, v45
	v_cvt_pk_bf16_f32 v51, v46, v47
	global_store_dwordx4 v[174:175], v[48:51], off nt
	v_pk_mul_f32 v[40:41], v[40:41], v[162:163] op_sel_hi:[1,0]
	v_pk_mul_f32 v[42:43], v[42:43], v[162:163] op_sel_hi:[1,0]
	v_pk_mul_f32 v[36:37], v[36:37], v[162:163] op_sel_hi:[1,0]
	v_pk_mul_f32 v[38:39], v[38:39], v[162:163] op_sel_hi:[1,0]
	v_pk_mul_f32 v[146:147], v[40:41], v[170:171] op_sel_hi:[1,0]
	v_pk_mul_f32 v[176:177], v[42:43], v[170:171] op_sel_hi:[1,0]
	v_pk_mul_f32 v[178:179], v[36:37], v[170:171] op_sel_hi:[1,0]
	v_pk_mul_f32 v[180:181], v[38:39], v[170:171] op_sel_hi:[1,0]
	v_exp_f32_e32 v146, v146
	v_exp_f32_e32 v147, v147
	v_exp_f32_e32 v176, v176
	v_exp_f32_e32 v177, v177
	v_exp_f32_e32 v178, v178
	v_exp_f32_e32 v179, v179
	v_exp_f32_e32 v180, v180
	v_exp_f32_e32 v181, v181
	v_pk_add_f32 v[146:147], v[146:147], v[168:169] op_sel_hi:[1,0]
	v_pk_add_f32 v[176:177], v[176:177], v[168:169] op_sel_hi:[1,0]
	v_pk_add_f32 v[178:179], v[178:179], v[168:169] op_sel_hi:[1,0]
	v_pk_add_f32 v[180:181], v[180:181], v[168:169] op_sel_hi:[1,0]
	v_rcp_f32_e32 v146, v146
	v_rcp_f32_e32 v147, v147
	v_rcp_f32_e32 v176, v176
	v_rcp_f32_e32 v177, v177
	v_rcp_f32_e32 v178, v178
	v_rcp_f32_e32 v179, v179
	v_rcp_f32_e32 v180, v180
	v_rcp_f32_e32 v181, v181
	v_pk_mul_f32 v[40:41], v[40:41], v[146:147]
	v_pk_mul_f32 v[42:43], v[42:43], v[176:177]
	v_pk_mul_f32 v[36:37], v[36:37], v[178:179]
	v_pk_mul_f32 v[38:39], v[38:39], v[180:181]
	v_cvt_pk_bf16_f32 v40, v40, v41
	v_cvt_pk_bf16_f32 v41, v42, v43
	v_cvt_pk_bf16_f32 v42, v36, v37
	v_cvt_pk_bf16_f32 v43, v38, v39
	global_store_dwordx4 v[174:175], v[40:43], off offset:256 nt
	v_lshl_add_u64 v[172:173], v[174:175], 0, s[100:101]
	v_pk_mul_f32 v[32:33], v[32:33], v[164:165] op_sel_hi:[1,0]
	v_pk_mul_f32 v[34:35], v[34:35], v[164:165] op_sel_hi:[1,0]
	v_pk_mul_f32 v[28:29], v[28:29], v[164:165] op_sel_hi:[1,0]
	v_pk_mul_f32 v[30:31], v[30:31], v[164:165] op_sel_hi:[1,0]
	v_pk_mul_f32 v[146:147], v[32:33], v[170:171] op_sel_hi:[1,0]
	v_pk_mul_f32 v[176:177], v[34:35], v[170:171] op_sel_hi:[1,0]
	v_pk_mul_f32 v[178:179], v[28:29], v[170:171] op_sel_hi:[1,0]
	v_pk_mul_f32 v[180:181], v[30:31], v[170:171] op_sel_hi:[1,0]
	v_exp_f32_e32 v146, v146
	v_exp_f32_e32 v147, v147
	v_exp_f32_e32 v176, v176
	v_exp_f32_e32 v177, v177
	v_exp_f32_e32 v178, v178
	v_exp_f32_e32 v179, v179
	v_exp_f32_e32 v180, v180
	v_exp_f32_e32 v181, v181
	v_pk_add_f32 v[146:147], v[146:147], v[168:169] op_sel_hi:[1,0]
	v_pk_add_f32 v[176:177], v[176:177], v[168:169] op_sel_hi:[1,0]
	v_pk_add_f32 v[178:179], v[178:179], v[168:169] op_sel_hi:[1,0]
	v_pk_add_f32 v[180:181], v[180:181], v[168:169] op_sel_hi:[1,0]
	v_rcp_f32_e32 v146, v146
	v_rcp_f32_e32 v147, v147
	v_rcp_f32_e32 v176, v176
	v_rcp_f32_e32 v177, v177
	v_rcp_f32_e32 v178, v178
	v_rcp_f32_e32 v179, v179
	v_rcp_f32_e32 v180, v180
	v_rcp_f32_e32 v181, v181
	v_pk_mul_f32 v[32:33], v[32:33], v[146:147]
	v_pk_mul_f32 v[34:35], v[34:35], v[176:177]
; __device__ __forceinline__ unsigned cvt_pk_bf16(float lo, float hi) { f32x2_t v = {lo, hi}; bf16x2_t b = __builtin_convertvector(v, bf16x2_t); return __builtin_bit_cast(unsigned, b); }
; __device__ __forceinline__ float sigmoid_f(float x) { return __builtin_amdgcn_rcpf(1.0f + __builtin_amdgcn_exp2f(-1.4426950408889634f * x)); }
; template <int ACT> __device__ __forceinline__ float act_f(float v) {
;     if (ACT == 1) return v * sigmoid_f(v);
;     template <int ACT, int AUX> __device__ __forceinline__ void run(const f32x4 (&acc)[2][2][4][2], const Unit& uu, int wr, int wc, int fr, int fq) const {
;     ...
;             for (int m = 0; m < 4; ++m) { const int r = row0 + ai * HALF + m * 16; const float rs = rsv[ai * 4 + m];
;                 bf16_t* rowp = O + (size_t)r * cfg::NC + col0; float s1 = 0.f, s2 = 0.f;
; #pragma unroll
;                 for (int bj = 0; bj < 2; ++bj) { f32x4 v0 = acc[ai][bj][m][0] * rs, v1 = acc[ai][bj][m][1] * rs;
; #pragma unroll
;                     for (int j = 0; j < 4; ++j) { v0[j] = act_f<ACT>(v0[j]); v1[j] = act_f<ACT>(v1[j]); }
;                     if (AUX == 4) {
;                         unsigned q[8];
; #pragma unroll
;                         for (int j = 0; j < 4; ++j) { q[j] = (unsigned)fminf(fmaxf(fmaf(v0[j], 255.0f, 0.5f), 1.0f), 255.0f); q[4 + j] = (unsigned)fminf(fmaxf(fmaf(v1[j], 255.0f, 0.5f), 1.0f), 255.0f); }
;                         u32x2 w8; w8.x = q[0] | (q[1] << 8) | (q[2] << 16) | (q[3] << 24); w8.y = q[4] | (q[5] << 8) | (q[6] << 16) | (q[7] << 24);
;                         __builtin_nontemporal_store(w8, (u32x2*)(g8 + ((size_t)((u.pn - 52) >> 4) * cfg::MT + r) * cfg::DM + ((u.pn - 52) & 15) * BM + wc * 32 + 8 * fq + bj * HALF));
;                     } else {
;                     u32x4 w; w.x = cvt_pk_bf16(v0[0], v0[1]); w.y = cvt_pk_bf16(v0[2], v0[3]); w.z = cvt_pk_bf16(v1[0], v1[1]); w.w = cvt_pk_bf16(v1[2], v1[3]);
;                     __builtin_nontemporal_store(w, (u32x4*)(rowp + bj * HALF)); }
	v_pk_mul_f32 v[28:29], v[28:29], v[178:179]
	v_pk_mul_f32 v[30:31], v[30:31], v[180:181]
	v_cvt_pk_bf16_f32 v32, v32, v33
	v_cvt_pk_bf16_f32 v33, v34, v35
	v_cvt_pk_bf16_f32 v34, v28, v29
	v_cvt_pk_bf16_f32 v35, v30, v31
	global_store_dwordx4 v[172:173], v[32:35], off nt
	v_pk_mul_f32 v[24:25], v[24:25], v[164:165] op_sel_hi:[1,0]
	v_pk_mul_f32 v[26:27], v[26:27], v[164:165] op_sel_hi:[1,0]
	v_pk_mul_f32 v[20:21], v[20:21], v[164:165] op_sel_hi:[1,0]
	v_pk_mul_f32 v[22:23], v[22:23], v[164:165] op_sel_hi:[1,0]
	v_pk_mul_f32 v[146:147], v[24:25], v[170:171] op_sel_hi:[1,0]
	v_pk_mul_f32 v[176:177], v[26:27], v[170:171] op_sel_hi:[1,0]
	v_pk_mul_f32 v[178:179], v[20:21], v[170:171] op_sel_hi:[1,0]
	v_pk_mul_f32 v[180:181], v[22:23], v[170:171] op_sel_hi:[1,0]
	v_exp_f32_e32 v146, v146
	v_exp_f32_e32 v147, v147
	v_exp_f32_e32 v176, v176
	v_exp_f32_e32 v177, v177
	v_exp_f32_e32 v178, v178
	v_exp_f32_e32 v179, v179
	v_exp_f32_e32 v180, v180
	v_exp_f32_e32 v181, v181
	v_pk_add_f32 v[146:147], v[146:147], v[168:169] op_sel_hi:[1,0]
	v_pk_add_f32 v[176:177], v[176:177], v[168:169] op_sel_hi:[1,0]
	v_pk_add_f32 v[178:179], v[178:179], v[168:169] op_sel_hi:[1,0]
	v_pk_add_f32 v[180:181], v[180:181], v[168:169] op_sel_hi:[1,0]
	v_rcp_f32_e32 v146, v146
	v_rcp_f32_e32 v147, v147
	v_rcp_f32_e32 v176, v176
	v_rcp_f32_e32 v177, v177
	v_rcp_f32_e32 v178, v178
	v_rcp_f32_e32 v179, v179
	v_rcp_f32_e32 v180, v180
	v_rcp_f32_e32 v181, v181
	v_pk_mul_f32 v[24:25], v[24:25], v[146:147]
	v_pk_mul_f32 v[26:27], v[26:27], v[176:177]
	v_pk_mul_f32 v[20:21], v[20:21], v[178:179]
	v_pk_mul_f32 v[22:23], v[22:23], v[180:181]
	v_cvt_pk_bf16_f32 v24, v24, v25
	v_cvt_pk_bf16_f32 v25, v26, v27
	v_cvt_pk_bf16_f32 v26, v20, v21
	v_cvt_pk_bf16_f32 v27, v22, v23
	global_store_dwordx4 v[172:173], v[24:27], off offset:256 nt
	v_lshl_add_u64 v[174:175], v[172:173], 0, s[100:101]
	v_pk_mul_f32 v[16:17], v[16:17], v[166:167] op_sel_hi:[1,0]
	v_pk_mul_f32 v[18:19], v[18:19], v[166:167] op_sel_hi:[1,0]
	v_pk_mul_f32 v[12:13], v[12:13], v[166:167] op_sel_hi:[1,0]
	v_pk_mul_f32 v[14:15], v[14:15], v[166:167] op_sel_hi:[1,0]
	v_pk_mul_f32 v[146:147], v[16:17], v[170:171] op_sel_hi:[1,0]
	v_pk_mul_f32 v[176:177], v[18:19], v[170:171] op_sel_hi:[1,0]
	v_pk_mul_f32 v[178:179], v[12:13], v[170:171] op_sel_hi:[1,0]
	v_pk_mul_f32 v[180:181], v[14:15], v[170:171] op_sel_hi:[1,0]
	v_exp_f32_e32 v146, v146
	v_exp_f32_e32 v147, v147
	v_exp_f32_e32 v176, v176
	v_exp_f32_e32 v177, v177
	v_exp_f32_e32 v178, v178
	v_exp_f32_e32 v179, v179
	v_exp_f32_e32 v180, v180
	v_exp_f32_e32 v181, v181
	v_pk_add_f32 v[146:147], v[146:147], v[168:169] op_sel_hi:[1,0]
	v_pk_add_f32 v[176:177], v[176:177], v[168:169] op_sel_hi:[1,0]
	v_pk_add_f32 v[178:179], v[178:179], v[168:169] op_sel_hi:[1,0]
	v_pk_add_f32 v[180:181], v[180:181], v[168:169] op_sel_hi:[1,0]
	v_rcp_f32_e32 v146, v146
	v_rcp_f32_e32 v147, v147
	v_rcp_f32_e32 v176, v176
	v_rcp_f32_e32 v177, v177
	v_rcp_f32_e32 v178, v178
	v_rcp_f32_e32 v179, v179
	v_rcp_f32_e32 v180, v180
	v_rcp_f32_e32 v181, v181
	v_pk_mul_f32 v[16:17], v[16:17], v[146:147]
	v_pk_mul_f32 v[18:19], v[18:19], v[176:177]
	v_pk_mul_f32 v[12:13], v[12:13], v[178:179]
	v_pk_mul_f32 v[14:15], v[14:15], v[180:181]
	v_cvt_pk_bf16_f32 v16, v16, v17
	v_cvt_pk_bf16_f32 v17, v18, v19
	v_cvt_pk_bf16_f32 v18, v12, v13
	v_cvt_pk_bf16_f32 v19, v14, v15
	global_store_dwordx4 v[174:175], v[16:19], off nt
	v_pk_mul_f32 v[8:9], v[8:9], v[166:167] op_sel_hi:[1,0]
	v_pk_mul_f32 v[10:11], v[10:11], v[166:167] op_sel_hi:[1,0]
	v_pk_mul_f32 v[4:5], v[4:5], v[166:167] op_sel_hi:[1,0]
	v_pk_mul_f32 v[6:7], v[6:7], v[166:167] op_sel_hi:[1,0]
	v_pk_mul_f32 v[146:147], v[8:9], v[170:171] op_sel_hi:[1,0]
	v_pk_mul_f32 v[176:177], v[10:11], v[170:171] op_sel_hi:[1,0]
	v_pk_mul_f32 v[178:179], v[4:5], v[170:171] op_sel_hi:[1,0]
	v_pk_mul_f32 v[180:181], v[6:7], v[170:171] op_sel_hi:[1,0]
	v_exp_f32_e32 v146, v146
	v_exp_f32_e32 v147, v147
	v_exp_f32_e32 v176, v176
	v_exp_f32_e32 v177, v177
	v_exp_f32_e32 v178, v178
	v_exp_f32_e32 v179, v179
	v_exp_f32_e32 v180, v180
	v_exp_f32_e32 v181, v181
	v_pk_add_f32 v[146:147], v[146:147], v[168:169] op_sel_hi:[1,0]
	v_pk_add_f32 v[176:177], v[176:177], v[168:169] op_sel_hi:[1,0]
	v_pk_add_f32 v[178:179], v[178:179], v[168:169] op_sel_hi:[1,0]
	v_pk_add_f32 v[180:181], v[180:181], v[168:169] op_sel_hi:[1,0]
	v_rcp_f32_e32 v146, v146
	v_rcp_f32_e32 v147, v147
	v_rcp_f32_e32 v176, v176
	v_rcp_f32_e32 v177, v177
	v_rcp_f32_e32 v178, v178
	v_rcp_f32_e32 v179, v179
	v_rcp_f32_e32 v180, v180
	v_rcp_f32_e32 v181, v181
	v_pk_mul_f32 v[8:9], v[8:9], v[146:147]
	v_pk_mul_f32 v[10:11], v[10:11], v[176:177]
	v_pk_mul_f32 v[4:5], v[4:5], v[178:179]
	v_pk_mul_f32 v[6:7], v[6:7], v[180:181]
	v_cvt_pk_bf16_f32 v8, v8, v9
	v_cvt_pk_bf16_f32 v9, v10, v11
	v_cvt_pk_bf16_f32 v10, v4, v5
	v_cvt_pk_bf16_f32 v11, v6, v7
	global_store_dwordx4 v[174:175], v[8:11], off offset:256 nt
